# v64 + LayerNorm wave reductions in P4/P7: the four in-row xor hops (8,4,2,1) done with DPP adds (row_ror, quad_perm) instead of ds_bpermute round trips; bit-identical sums
# speedup vs baseline: 1.0034x; 1.0034x over previous
; DI float bflo(unsigned w) { return __uint_as_float(w << 16); }
; DI float bfhi(unsigned w) { return __uint_as_float(w & 0xffff0000u); }
; DI void p4_ln_router(const Ctx& c) {
;     ...
;         for (int tt = 0; tt < 2; ++tt) { const int tl = 2 * w + tt, tok = tokbase + pass * 16 + tl;
;             const u32x2* src = (const u32x2*)(y1 + (size_t)tok * D); f32x4 v[8]; float s = 0.f;
; #pragma unroll
;             for (int i = 0; i < 8; ++i) { const u32x2 yv = src[i * 64 + lane]; v[i] = (f32x4){bflo(yv.x), bfhi(yv.x), bflo(yv.y), bfhi(yv.y)}; s += (v[i][0] + v[i][1]) + (v[i][2] + v[i][3]); }
; #pragma unroll
;             for (int o = 32; o >= 1; o >>= 1) s += __shfl_xor(s, o);
.LBB0_443:
	s_or_b32 s36, s24, s5
	s_add_i32 s24, s31, s36
	s_ashr_i32 s25, s24, 31
	s_lshl_b64 s[26:27], s[24:25], 12
	v_lshl_add_u64 v[0:1], v[50:51], 0, s[26:27]
	global_load_dwordx2 v[2:3], v[0:1], off offset:512
	global_load_dwordx2 v[4:5], v[0:1], off
	global_load_dwordx2 v[6:7], v[0:1], off offset:1024
	global_load_dwordx2 v[8:9], v[0:1], off offset:1536
	global_load_dwordx2 v[10:11], v[0:1], off offset:2048
	global_load_dwordx2 v[12:13], v[0:1], off offset:2560
	global_load_dwordx2 v[68:69], v[0:1], off offset:3072
	global_load_dwordx2 v[70:71], v[0:1], off offset:3584
	s_waitcnt vmcnt(7)
	v_lshlrev_b32_e32 v63, 16, v2
	s_waitcnt vmcnt(6)
	v_lshlrev_b32_e32 v62, 16, v4
	v_and_b32_e32 v61, 0xffff0000, v2
	v_and_b32_e32 v60, 0xffff0000, v4
	v_lshlrev_b32_e32 v67, 16, v3
	v_lshlrev_b32_e32 v66, 16, v5
	v_and_b32_e32 v65, 0xffff0000, v3
	v_and_b32_e32 v64, 0xffff0000, v5
	s_waitcnt vmcnt(5)
	v_lshlrev_b32_e32 v57, 16, v7
	v_lshlrev_b32_e32 v56, 16, v6
	v_and_b32_e32 v59, 0xffff0000, v7
	v_and_b32_e32 v58, 0xffff0000, v6
	s_waitcnt vmcnt(4)
	v_lshlrev_b32_e32 v22, 16, v8
	v_and_b32_e32 v23, 0xffff0000, v8
	v_lshlrev_b32_e32 v54, 16, v9
	v_and_b32_e32 v55, 0xffff0000, v9
	s_waitcnt vmcnt(1)
	v_lshlrev_b32_e32 v6, 16, v68
	v_and_b32_e32 v7, 0xffff0000, v68
	v_lshlrev_b32_e32 v8, 16, v69
	v_and_b32_e32 v9, 0xffff0000, v69
	s_waitcnt vmcnt(0)
	v_lshlrev_b32_e32 v2, 16, v70
	v_and_b32_e32 v3, 0xffff0000, v70
	v_lshlrev_b32_e32 v5, 16, v71
	v_and_b32_e32 v1, 0xffff0000, v71
	v_pk_add_f32 v[68:69], v[62:63], v[60:61]
	v_pk_add_f32 v[70:71], v[66:67], v[64:65]
	v_pk_add_f32 v[72:73], v[56:57], v[58:59]
	v_add_f32_e32 v4, v6, v7
	v_add_f32_e32 v0, v8, v9
	v_pk_add_f32 v[68:69], v[68:69], v[70:71]
	v_and_b32_e32 v15, 0xffff0000, v10
	v_pk_add_f32 v[70:71], v[72:73], v[72:73] op_sel:[0,1] op_sel_hi:[1,0]
	v_pk_add_f32 v[76:77], v[4:5], v[0:1]
	v_add_f32_e32 v0, 0, v68
	v_lshlrev_b32_e32 v19, 16, v10
	v_lshlrev_b32_e32 v21, 16, v11
	v_and_b32_e32 v17, 0xffff0000, v11
	v_add_f32_e32 v20, v22, v23
	v_add_f32_e32 v16, v54, v55
	v_mov_b32_e32 v71, v15
	v_add_f32_e32 v18, v0, v69
	v_lshlrev_b32_e32 v11, 16, v13
	v_lshlrev_b32_e32 v10, 16, v12
	v_and_b32_e32 v13, 0xffff0000, v13
	v_and_b32_e32 v12, 0xffff0000, v12
	v_pk_add_f32 v[72:73], v[20:21], v[16:17]
	v_pk_add_f32 v[68:69], v[18:19], v[70:71]
	v_pk_add_f32 v[74:75], v[10:11], v[12:13]
	v_pk_add_f32 v[68:69], v[68:69], v[72:73]
	v_pk_add_f32 v[74:75], v[74:75], v[74:75] op_sel:[0,1] op_sel_hi:[1,0]
	v_pk_add_f32 v[68:69], v[68:69], v[68:69] op_sel:[0,1] op_sel_hi:[1,0]
	v_mov_b32_e32 v75, v3
	v_mov_b32_e32 v69, v2
	v_pk_add_f32 v[68:69], v[68:69], v[74:75]
	s_nop 0
	v_pk_add_f32 v[68:69], v[68:69], v[76:77]
	s_nop 0
	v_add_f32_e32 v0, v68, v69
	ds_bpermute_b32 v4, v83, v0
	s_waitcnt lgkmcnt(0)
	v_add_f32_e32 v0, v0, v4
	ds_bpermute_b32 v4, v84, v0
	s_waitcnt lgkmcnt(0)
; DI void p4_ln_router(const Ctx& c) {
;     ...
;             for (int o = 32; o >= 1; o >>= 1) s += __shfl_xor(s, o);
;             const float mean = s * (1.0f / D); float qv = 0.f;
; #pragma unroll
;             for (int i = 0; i < 8; ++i) { const f32x4 dl = v[i] - mean; qv += (dl[0] * dl[0] + dl[1] * dl[1]) + (dl[2] * dl[2] + dl[3] * dl[3]); }
; #pragma unroll
;             for (int o = 32; o >= 1; o >>= 1) qv += __shfl_xor(qv, o);
;             const float rstd = rsqrtf(qv * (1.0f / D) + LN_EPS);
;             if (lane == 0) { st1[2 * tok] = mean; st1[2 * tok + 1] = rstd; }
	v_add_f32_e32 v0, v0, v4
	s_nop 1
	v_add_f32_dpp v0, v0, v0 row_ror:8 row_mask:0xf bank_mask:0xf
	s_nop 1
	v_add_f32_dpp v0, v0, v0 row_ror:4 row_mask:0xf bank_mask:0xf
	s_nop 1
	v_add_f32_dpp v0, v0, v0 quad_perm:[2,3,0,1] row_mask:0xf bank_mask:0xf
	s_nop 1
	v_add_f32_dpp v0, v0, v0 quad_perm:[1,0,3,2] row_mask:0xf bank_mask:0xf
	v_fmac_f32_e32 v64, 0xba000000, v0
	v_fmac_f32_e32 v60, 0xba000000, v0
	v_fmac_f32_e32 v65, 0xba000000, v0
	v_fmac_f32_e32 v61, 0xba000000, v0
	v_fmac_f32_e32 v59, 0xba000000, v0
	v_fmac_f32_e32 v57, 0xba000000, v0
	v_fmac_f32_e32 v58, 0xba000000, v0
	v_fmac_f32_e32 v66, 0xba000000, v0
	v_fmac_f32_e32 v62, 0xba000000, v0
	v_fmac_f32_e32 v67, 0xba000000, v0
	v_fmac_f32_e32 v63, 0xba000000, v0
	v_fmac_f32_e32 v56, 0xba000000, v0
	v_pk_mul_f32 v[68:69], v[60:61], v[60:61]
	v_pk_mul_f32 v[72:73], v[64:65], v[64:65]
	v_mov_b32_e32 v78, v57
	v_mov_b32_e32 v79, v59
	v_mov_b32_e32 v57, v58
	v_pk_fma_f32 v[68:69], v[62:63], v[62:63], v[68:69]
	v_pk_fma_f32 v[72:73], v[66:67], v[66:67], v[72:73]
	v_pk_mul_f32 v[74:75], v[78:79], v[78:79]
	v_pk_mul_f32 v[76:77], v[56:57], v[56:57]
	v_fmac_f32_e32 v54, 0xba000000, v0
	v_fmac_f32_e32 v22, 0xba000000, v0
	v_pk_add_f32 v[68:69], v[68:69], v[72:73]
	v_pk_mov_b32 v[72:73], v[76:77], v[74:75] op_sel:[1,0]
	v_mov_b32_e32 v77, v75
	v_fmac_f32_e32 v55, 0xba000000, v0
	v_fmac_f32_e32 v23, 0xba000000, v0
	v_fmac_f32_e32 v15, 0xba000000, v0
	v_fmac_f32_e32 v13, 0xba000000, v0
	v_fmac_f32_e32 v11, 0xba000000, v0
	v_fmac_f32_e32 v12, 0xba000000, v0
	v_mul_f32_e32 v4, v22, v22
	v_mul_f32_e32 v14, v54, v54
	v_pk_add_f32 v[72:73], v[72:73], v[76:77]
	v_fmac_f32_e32 v17, 0xba000000, v0
	v_fmac_f32_e32 v21, 0xba000000, v0
	v_fmac_f32_e32 v19, 0xba000000, v0
	v_fmac_f32_e32 v10, 0xba000000, v0
	v_mov_b32_e32 v70, v11
	v_mov_b32_e32 v71, v13
	v_mov_b32_e32 v11, v12
	v_pk_fma_f32 v[116:117], v[22:23], v[22:23], v[4:5] op_sel_hi:[1,1,0]
	v_pk_fma_f32 v[118:119], v[54:55], v[54:55], v[14:15] op_sel_hi:[1,1,0]
	v_pk_add_f32 v[68:69], v[68:69], v[68:69] op_sel_hi:[0,1]
	v_pk_add_f32 v[72:73], v[72:73], v[72:73] op_sel_hi:[0,1]
	v_pk_mul_f32 v[120:121], v[70:71], v[70:71]
	v_pk_mul_f32 v[122:123], v[10:11], v[10:11]
	v_mul_f32_e32 v116, v19, v19
	v_mul_f32_e32 v118, v15, v15
	v_mul_f32_e32 v68, v17, v17
	v_mul_f32_e32 v72, v21, v21
	v_fmac_f32_e32 v6, 0xba000000, v0
	v_fmac_f32_e32 v8, 0xba000000, v0
	v_pk_mov_b32 v[74:75], v[122:123], v[120:121] op_sel:[1,0]
	v_mov_b32_e32 v123, v121
	v_pk_add_f32 v[76:77], v[116:117], v[118:119]
	v_pk_add_f32 v[68:69], v[72:73], v[68:69]
	v_fmac_f32_e32 v7, 0xba000000, v0
	v_mul_f32_e32 v4, v6, v6
	v_fmac_f32_e32 v9, 0xba000000, v0
	v_pk_add_f32 v[74:75], v[74:75], v[122:123]
	v_pk_add_f32 v[68:69], v[76:77], v[68:69]
	v_pk_fma_f32 v[72:73], v[6:7], v[6:7], v[4:5] op_sel_hi:[1,1,0]
	v_mul_f32_e32 v4, v8, v8
	v_pk_add_f32 v[74:75], v[74:75], v[74:75] op_sel_hi:[0,1]
	v_pk_add_f32 v[68:69], v[68:69], v[68:69] op_sel_hi:[0,1]
	v_pk_fma_f32 v[76:77], v[8:9], v[8:9], v[4:5] op_sel_hi:[1,1,0]
	v_fmac_f32_e32 v1, 0xba000000, v0
	v_fmac_f32_e32 v5, 0xba000000, v0
	v_fmac_f32_e32 v3, 0xba000000, v0
	v_fmac_f32_e32 v2, 0xba000000, v0
	v_mul_f32_e32 v72, v2, v2
	v_mul_f32_e32 v76, v3, v3
	v_mul_f32_e32 v74, v5, v5
	v_mul_f32_e32 v68, v1, v1
	v_pk_add_f32 v[72:73], v[72:73], v[76:77]
	v_pk_add_f32 v[68:69], v[74:75], v[68:69]
	s_nop 0
	v_pk_add_f32 v[68:69], v[72:73], v[68:69]
	s_nop 0
	v_add_f32_e32 v4, v68, v69
	ds_bpermute_b32 v11, v83, v4
	s_waitcnt lgkmcnt(0)
	v_add_f32_e32 v4, v4, v11
	ds_bpermute_b32 v11, v84, v4
	s_waitcnt lgkmcnt(0)
	v_add_f32_e32 v4, v4, v11
	s_nop 1
	v_add_f32_dpp v4, v4, v4 row_ror:8 row_mask:0xf bank_mask:0xf
	s_nop 1
	v_add_f32_dpp v4, v4, v4 row_ror:4 row_mask:0xf bank_mask:0xf
	s_nop 1
	v_add_f32_dpp v4, v4, v4 quad_perm:[2,3,0,1] row_mask:0xf bank_mask:0xf
	s_nop 1
	v_add_f32_dpp v4, v4, v4 quad_perm:[1,0,3,2] row_mask:0xf bank_mask:0xf
	v_fmamk_f32 v4, v4, 0x3a000000, v110
	v_mul_f32_e32 v11, 0x4b800000, v4
	v_cmp_gt_f32_e32 vcc, s6, v4
	s_nop 1
	v_cndmask_b32_e32 v4, v4, v11, vcc
	v_rsq_f32_e32 v4, v4
	s_nop 0
	v_mul_f32_e32 v11, 0x45800000, v4
	v_cndmask_b32_e32 v4, v4, v11, vcc
	s_and_saveexec_b64 s[26:27], s[10:11]
	s_cbranch_execz .LBB0_442
	s_lshl_b32 s38, s24, 1
	s_ashr_i32 s39, s38, 31
	s_lshl_b64 s[38:39], s[38:39], 2
	s_add_u32 s38, s3, s38
	v_mul_f32_e32 v68, 0x3a000000, v0
	s_addc_u32 s39, s71, s39
	v_mov_b32_e32 v69, v4
	global_store_dwordx2 v25, v[68:69], s[38:39]
	s_branch .LBB0_442

; DI float bflo(unsigned w) { return __uint_as_float(w << 16); }
; DI float bfhi(unsigned w) { return __uint_as_float(w & 0xffff0000u); }
; DI void p7_ln2(const Ctx& c) {
;     ...
;         for (int i = 0; i < 4; ++i) { const int d = (i * 64 + lane) * 8; const u32x4 yr = *(const u32x4*)(y1 + (size_t)tok * D + d);
;             const f32x4 y0 = {bflo(yr.x), bfhi(yr.x), bflo(yr.y), bfhi(yr.y)}, y1v = {bflo(yr.z), bfhi(yr.z), bflo(yr.w), bfhi(yr.w)};
;             const f32x4 g0 = *(const f32x4*)(l1w + d), g1 = *(const f32x4*)(l1w + d + 4), b0 = *(const f32x4*)(l1b + d), b1 = *(const f32x4*)(l1b + d + 4);
;             f32x4 a0 = ((y0 - mean1) * rstd1 * g0 + b0) * DN_ALPHA, a1 = ((y1v - mean1) * rstd1 * g1 + b1) * DN_ALPHA;
; #pragma unroll
;             for (int k = 0; k < 4; ++k) { const u32x4 v = *(const u32x4*)(yb + ((size_t)tok * 4 + k) * D + d);
;                 a0[0] += bflo(v.x); a0[1] += bfhi(v.x); a0[2] += bflo(v.y); a0[3] += bfhi(v.y); a1[0] += bflo(v.z); a1[1] += bfhi(v.z); a1[2] += bflo(v.w); a1[3] += bfhi(v.w); }
;             z[2 * i] = a0; z[2 * i + 1] = a1; s += ((a0[0] + a0[1]) + (a0[2] + a0[3])) + ((a1[0] + a1[1]) + (a1[2] + a1[3])); }
.LBB0_977:
	v_lshl_add_u64 v[72:73], s[34:35], 0, v[70:71]
	v_add_co_u32_e64 v86, s[10:11], s24, v72
	s_waitcnt lgkmcnt(0)
	v_lshl_add_u64 v[0:1], s[34:35], 0, v[62:63]
	v_addc_co_u32_e64 v87, s[10:11], 0, v73, s[10:11]
	global_load_dwordx4 v[16:19], v[86:87], off
	v_add_co_u32_e64 v2, s[10:11], s25, v0
	s_nop 1
	v_addc_co_u32_e64 v3, s[10:11], 0, v1, s[10:11]
	v_add_co_u32_e64 v0, s[10:11], s26, v0
	global_load_dwordx4 v[78:81], v[2:3], off
	s_nop 0
	v_addc_co_u32_e64 v1, s[10:11], 0, v1, s[10:11]
	s_add_i32 s10, s5, s13
	s_ashr_i32 s11, s10, 31
	global_load_dwordx4 v[88:91], v[0:1], off offset:-4096
	global_load_dwordx4 v[102:105], v[0:1], off
	s_lshl_b64 s[10:11], s[10:11], 2
	s_add_u32 s10, s3, s10
	s_addc_u32 s11, s71, s11
	global_load_dwordx2 v[82:83], v58, s[10:11]
	global_load_dwordx4 v[106:109], v[2:3], off offset:-4096
	global_load_dwordx4 v[74:77], v[26:27], off
	global_load_dwordx4 v[110:113], v[24:25], off
	global_load_dwordx4 v[114:117], v[24:25], off offset:16
	global_load_dwordx4 v[118:121], v[26:27], off offset:16
	global_load_dwordx4 v[12:15], v[24:25], off offset:2064
	global_load_dwordx4 v[122:125], v[24:25], off offset:2048
	v_lshl_add_u64 v[0:1], s[34:35], 0, v[64:65]
	v_add_co_u32_e64 v4, s[10:11], s25, v0
	s_waitcnt vmcnt(11)
	v_lshlrev_b32_e32 v59, 16, v16
	v_addc_co_u32_e64 v5, s[10:11], 0, v1, s[10:11]
	v_add_co_u32_e64 v84, s[10:11], s26, v0
	v_and_b32_e32 v101, 0xffff0000, v16
	s_nop 0
	v_addc_co_u32_e64 v85, s[10:11], 0, v1, s[10:11]
	global_load_dwordx4 v[130:133], v[86:87], off offset:1024
	global_load_dwordx4 v[8:11], v[4:5], off offset:-4096
	global_load_dwordx4 v[0:3], v[4:5], off
	s_nop 0
	global_load_dwordx4 v[4:7], v[84:85], off offset:-4096
	v_lshlrev_b32_e32 v134, 16, v17
	v_and_b32_e32 v135, 0xffff0000, v17
	s_waitcnt vmcnt(11)
	v_sub_f32_e32 v135, v135, v82
	v_sub_f32_e32 v134, v134, v82
	v_sub_f32_e32 v137, v101, v82
	v_sub_f32_e32 v136, v59, v82
	v_pk_mul_f32 v[136:137], v[82:83], v[136:137] op_sel:[1,0]
	v_pk_mul_f32 v[134:135], v[82:83], v[134:135] op_sel:[1,0]
	s_waitcnt vmcnt(10)
	v_lshlrev_b32_e32 v142, 16, v106
	v_and_b32_e32 v143, 0xffff0000, v106
	v_lshlrev_b32_e32 v106, 16, v107
	v_and_b32_e32 v107, 0xffff0000, v107
	s_waitcnt vmcnt(8)
	v_pk_fma_f32 v[76:77], v[112:113], v[134:135], v[76:77]
	v_pk_fma_f32 v[74:75], v[110:111], v[136:137], v[74:75]
	v_lshlrev_b32_e32 v16, 16, v78
	v_and_b32_e32 v17, 0xffff0000, v78
	v_lshlrev_b32_e32 v78, 16, v79
	v_and_b32_e32 v79, 0xffff0000, v79
	v_pk_fma_f32 v[74:75], v[74:75], s[14:15], v[142:143] op_sel_hi:[1,0,1]
	v_pk_fma_f32 v[76:77], v[76:77], s[14:15], v[106:107] op_sel_hi:[1,0,1]
	v_lshlrev_b32_e32 v140, 16, v18
	v_and_b32_e32 v141, 0xffff0000, v18
	v_lshlrev_b32_e32 v138, 16, v19
	v_and_b32_e32 v139, 0xffff0000, v19
	v_lshlrev_b32_e32 v18, 16, v88
	v_and_b32_e32 v19, 0xffff0000, v88
	v_lshlrev_b32_e32 v88, 16, v89
	v_and_b32_e32 v89, 0xffff0000, v89
	v_pk_add_f32 v[16:17], v[74:75], v[16:17]
	v_pk_add_f32 v[74:75], v[76:77], v[78:79]
	v_lshlrev_b32_e32 v92, 16, v102
	v_and_b32_e32 v93, 0xffff0000, v102
	v_lshlrev_b32_e32 v102, 16, v103
	v_pk_add_f32 v[16:17], v[16:17], v[18:19]
	v_pk_add_f32 v[18:19], v[74:75], v[88:89]
	v_and_b32_e32 v103, 0xffff0000, v103
	v_pk_add_f32 v[74:75], v[16:17], v[92:93]
	v_pk_add_f32 v[76:77], v[18:19], v[102:103]
	global_load_dwordx4 v[16:19], v[84:85], off
	v_sub_f32_e32 v141, v141, v82
	v_sub_f32_e32 v140, v140, v82
	v_pk_mul_f32 v[140:141], v[82:83], v[140:141] op_sel:[1,0]
	v_lshlrev_b32_e32 v78, 16, v108
	s_waitcnt vmcnt(7)
	v_pk_fma_f32 v[112:113], v[114:115], v[140:141], v[118:119]
	v_and_b32_e32 v79, 0xffff0000, v108
	v_pk_fma_f32 v[78:79], v[112:113], s[14:15], v[78:79] op_sel_hi:[1,0,1]
	v_lshlrev_b32_e32 v84, 16, v80
	v_and_b32_e32 v85, 0xffff0000, v80
	v_sub_f32_e32 v139, v139, v82
	v_sub_f32_e32 v138, v138, v82
	v_pk_add_f32 v[78:79], v[78:79], v[84:85]
	v_lshlrev_b32_e32 v84, 16, v90
	v_and_b32_e32 v85, 0xffff0000, v90
	v_pk_mul_f32 v[138:139], v[82:83], v[138:139] op_sel:[1,0]
	v_pk_add_f32 v[78:79], v[78:79], v[84:85]
	v_lshlrev_b32_e32 v84, 16, v104
	v_and_b32_e32 v85, 0xffff0000, v104
	v_pk_fma_f32 v[110:111], v[116:117], v[138:139], v[120:121]
	v_pk_add_f32 v[78:79], v[78:79], v[84:85]
	v_lshlrev_b32_e32 v84, 16, v109
	v_and_b32_e32 v85, 0xffff0000, v109
	v_pk_fma_f32 v[84:85], v[110:111], s[14:15], v[84:85] op_sel_hi:[1,0,1]
	v_lshlrev_b32_e32 v80, 16, v81
	v_and_b32_e32 v81, 0xffff0000, v81
	v_pk_add_f32 v[80:81], v[84:85], v[80:81]
	v_lshlrev_b32_e32 v84, 16, v91
	v_and_b32_e32 v85, 0xffff0000, v91
	v_pk_add_f32 v[80:81], v[80:81], v[84:85]
	v_lshlrev_b32_e32 v84, 16, v105
	v_and_b32_e32 v85, 0xffff0000, v105
	v_pk_add_f32 v[80:81], v[80:81], v[84:85]
	v_mov_b32_e32 v84, v78
	v_mov_b32_e32 v85, v74
	v_mov_b32_e32 v88, v79
	v_mov_b32_e32 v89, v75
	v_pk_add_f32 v[84:85], v[84:85], v[88:89]
	v_mov_b32_e32 v88, v80
	v_mov_b32_e32 v89, v76
	v_mov_b32_e32 v90, v81
	v_mov_b32_e32 v91, v77
	v_pk_add_f32 v[88:89], v[88:89], v[90:91]
	s_waitcnt vmcnt(4)
	v_lshlrev_b32_e32 v59, 16, v130
	v_pk_add_f32 v[84:85], v[84:85], v[88:89]
	v_sub_f32_e32 v90, v59, v82
	v_pk_add_f32 v[88:89], v[84:85], v[84:85] op_sel:[0,1] op_sel_hi:[1,0]
	v_lshlrev_b32_e32 v84, 16, v131
	v_and_b32_e32 v89, 0xffff0000, v130
	v_and_b32_e32 v85, 0xffff0000, v131
	v_sub_f32_e32 v85, v85, v82
	v_sub_f32_e32 v84, v84, v82
	v_sub_f32_e32 v91, v89, v82
	v_lshlrev_b32_e32 v101, 16, v132
	v_and_b32_e32 v102, 0xffff0000, v132
	v_lshlrev_b32_e32 v103, 16, v133
	v_pk_mul_f32 v[90:91], v[82:83], v[90:91] op_sel:[1,0]
	v_pk_mul_f32 v[84:85], v[82:83], v[84:85] op_sel:[1,0]
	v_and_b32_e32 v104, 0xffff0000, v133
	v_pk_fma_f32 v[92:93], v[124:125], v[84:85], v[150:151]
	v_pk_fma_f32 v[84:85], v[122:123], v[90:91], v[148:149]
	v_sub_f32_e32 v90, v103, v82
	v_sub_f32_e32 v103, v102, v82
	v_sub_f32_e32 v102, v101, v82
	v_sub_f32_e32 v91, v104, v82
	v_pk_mul_f32 v[106:107], v[82:83], v[102:103] op_sel:[1,0]
	global_load_dwordx4 v[102:105], v[86:87], off offset:2048
	v_pk_fma_f32 v[122:123], v[12:13], v[106:107], v[144:145]
	v_pk_mul_f32 v[90:91], v[82:83], v[90:91] op_sel:[1,0]
	s_waitcnt vmcnt(4)
; DI float bflo(unsigned w) { return __uint_as_float(w << 16); }
; DI float bfhi(unsigned w) { return __uint_as_float(w & 0xffff0000u); }
; DI void p7_ln2(const Ctx& c) {
;     ...
;         for (int i = 0; i < 4; ++i) { const int d = (i * 64 + lane) * 8; const u32x4 yr = *(const u32x4*)(y1 + (size_t)tok * D + d);
;             const f32x4 y0 = {bflo(yr.x), bfhi(yr.x), bflo(yr.y), bfhi(yr.y)}, y1v = {bflo(yr.z), bfhi(yr.z), bflo(yr.w), bfhi(yr.w)};
;             const f32x4 g0 = *(const f32x4*)(l1w + d), g1 = *(const f32x4*)(l1w + d + 4), b0 = *(const f32x4*)(l1b + d), b1 = *(const f32x4*)(l1b + d + 4);
;             f32x4 a0 = ((y0 - mean1) * rstd1 * g0 + b0) * DN_ALPHA, a1 = ((y1v - mean1) * rstd1 * g1 + b1) * DN_ALPHA;
; #pragma unroll
;             for (int k = 0; k < 4; ++k) { const u32x4 v = *(const u32x4*)(yb + ((size_t)tok * 4 + k) * D + d);
;                 a0[0] += bflo(v.x); a0[1] += bfhi(v.x); a0[2] += bflo(v.y); a0[3] += bfhi(v.y); a1[0] += bflo(v.z); a1[1] += bfhi(v.z); a1[2] += bflo(v.w); a1[3] += bfhi(v.w); }
;             z[2 * i] = a0; z[2 * i + 1] = a1; s += ((a0[0] + a0[1]) + (a0[2] + a0[3])) + ((a1[0] + a1[1]) + (a1[2] + a1[3])); }
	v_lshlrev_b32_e32 v12, 16, v8
	v_and_b32_e32 v13, 0xffff0000, v8
	v_lshlrev_b32_e32 v8, 16, v9
	v_and_b32_e32 v9, 0xffff0000, v9
	v_pk_fma_f32 v[90:91], v[14:15], v[90:91], v[146:147]
	v_pk_fma_f32 v[12:13], v[84:85], s[14:15], v[12:13] op_sel_hi:[1,0,1]
	s_waitcnt vmcnt(3)
	v_lshlrev_b32_e32 v14, 16, v0
	v_and_b32_e32 v15, 0xffff0000, v0
	v_pk_fma_f32 v[8:9], v[92:93], s[14:15], v[8:9] op_sel_hi:[1,0,1]
	v_lshlrev_b32_e32 v0, 16, v1
	v_and_b32_e32 v1, 0xffff0000, v1
	v_pk_add_f32 v[12:13], v[12:13], v[14:15]
	s_waitcnt vmcnt(2)
	v_lshlrev_b32_e32 v14, 16, v4
	v_and_b32_e32 v15, 0xffff0000, v4
	v_pk_add_f32 v[0:1], v[8:9], v[0:1]
	v_lshlrev_b32_e32 v4, 16, v5
	v_and_b32_e32 v5, 0xffff0000, v5
	v_lshl_add_u64 v[124:125], s[34:35], 0, v[66:67]
	v_pk_add_f32 v[0:1], v[0:1], v[4:5]
	s_waitcnt vmcnt(1)
	v_lshlrev_b32_e32 v4, 16, v17
	v_and_b32_e32 v5, 0xffff0000, v17
	v_add_co_u32_e64 v22, s[10:11], s25, v124
	v_pk_add_f32 v[0:1], v[0:1], v[4:5]
	v_lshlrev_b32_e32 v4, 16, v10
	v_and_b32_e32 v5, 0xffff0000, v10
	v_addc_co_u32_e64 v23, s[10:11], 0, v125, s[10:11]
	v_pk_fma_f32 v[4:5], v[122:123], s[14:15], v[4:5] op_sel_hi:[1,0,1]
	v_lshlrev_b32_e32 v8, 16, v2
	v_and_b32_e32 v9, 0xffff0000, v2
	v_pk_add_f32 v[4:5], v[4:5], v[8:9]
	v_add_co_u32_e64 v8, s[10:11], s26, v124
	v_lshlrev_b32_e32 v84, 16, v16
	v_and_b32_e32 v85, 0xffff0000, v16
	v_addc_co_u32_e64 v9, s[10:11], 0, v125, s[10:11]
	v_lshlrev_b32_e32 v16, 16, v6
	v_and_b32_e32 v17, 0xffff0000, v6
	global_load_dwordx4 v[122:125], v[8:9], off offset:-4096
	global_load_dwordx4 v[126:129], v[8:9], off
	v_pk_add_f32 v[4:5], v[4:5], v[16:17]
	v_lshlrev_b32_e32 v8, 16, v18
	v_and_b32_e32 v9, 0xffff0000, v18
	v_pk_add_f32 v[4:5], v[4:5], v[8:9]
	v_lshlrev_b32_e32 v8, 16, v11
	v_and_b32_e32 v9, 0xffff0000, v11
	v_pk_fma_f32 v[8:9], v[90:91], s[14:15], v[8:9] op_sel_hi:[1,0,1]
	v_lshlrev_b32_e32 v2, 16, v3
	v_and_b32_e32 v3, 0xffff0000, v3
	v_pk_add_f32 v[20:21], v[12:13], v[14:15]
	global_load_dwordx4 v[12:15], v[22:23], off offset:-4096
	v_pk_add_f32 v[2:3], v[8:9], v[2:3]
	v_lshlrev_b32_e32 v6, 16, v7
	v_and_b32_e32 v7, 0xffff0000, v7
	v_pk_add_f32 v[84:85], v[20:21], v[84:85]
	v_pk_add_f32 v[2:3], v[2:3], v[6:7]
	v_lshlrev_b32_e32 v6, 16, v19
	v_and_b32_e32 v7, 0xffff0000, v19
	global_load_dwordx4 v[16:19], v[86:87], off offset:3072
	v_pk_add_f32 v[2:3], v[2:3], v[6:7]
	global_load_dwordx4 v[20:23], v[22:23], off
	v_mov_b32_e32 v6, v84
	v_mov_b32_e32 v7, v0
	v_mov_b32_e32 v8, v85
	v_mov_b32_e32 v9, v1
	v_pk_add_f32 v[6:7], v[6:7], v[8:9]
	v_mov_b32_e32 v8, v5
	v_pk_add_f32 v[90:91], v[6:7], v[6:7] op_sel:[0,1] op_sel_hi:[1,0]
	v_mov_b32_e32 v6, v4
	v_mov_b32_e32 v7, v2
	v_mov_b32_e32 v9, v3
	v_pk_add_f32 v[6:7], v[6:7], v[8:9]
	v_lshl_add_u64 v[134:135], s[34:35], 0, v[68:69]
	v_pk_add_f32 v[92:93], v[6:7], v[6:7] op_sel:[0,1] op_sel_hi:[1,0]
	s_waitcnt vmcnt(5)
	v_lshlrev_b32_e32 v8, 16, v102
	v_and_b32_e32 v9, 0xffff0000, v102
	v_lshlrev_b32_e32 v6, 16, v103
	v_and_b32_e32 v7, 0xffff0000, v103
	v_sub_f32_e32 v7, v7, v82
	v_sub_f32_e32 v6, v6, v82
	v_sub_f32_e32 v9, v9, v82
	v_sub_f32_e32 v8, v8, v82
	v_lshlrev_b32_e32 v59, 16, v104
	v_and_b32_e32 v86, 0xffff0000, v104
	v_lshlrev_b32_e32 v87, 16, v105
	v_and_b32_e32 v89, 0xffff0000, v105
	v_pk_mul_f32 v[8:9], v[82:83], v[8:9] op_sel:[1,0]
	v_pk_mul_f32 v[6:7], v[82:83], v[6:7] op_sel:[1,0]
	v_add_co_u32_e64 v130, s[10:11], s25, v134
	s_waitcnt vmcnt(5)
	v_pk_fma_f32 v[10:11], v[158:159], v[6:7], v[166:167]
	v_pk_fma_f32 v[6:7], v[156:157], v[8:9], v[164:165]
	v_sub_f32_e32 v9, v89, v82
	v_sub_f32_e32 v8, v87, v82
	v_sub_f32_e32 v87, v86, v82
	v_sub_f32_e32 v86, v59, v82
	v_pk_mul_f32 v[86:87], v[82:83], v[86:87] op_sel:[1,0]
	v_pk_mul_f32 v[8:9], v[82:83], v[8:9] op_sel:[1,0]
	v_pk_fma_f32 v[86:87], v[152:153], v[86:87], v[160:161]
	v_pk_fma_f32 v[142:143], v[154:155], v[8:9], v[162:163]
	v_addc_co_u32_e64 v131, s[10:11], 0, v135, s[10:11]
	v_add_co_u32_e64 v138, s[10:11], s26, v134
	global_load_dwordx4 v[118:121], v[130:131], off offset:-4096
	s_nop 0
	global_load_dwordx4 v[130:133], v[130:131], off
	v_addc_co_u32_e64 v139, s[10:11], 0, v135, s[10:11]
	global_load_dwordx4 v[134:137], v[138:139], off offset:-4096
	s_waitcnt vmcnt(5)
	v_lshlrev_b32_e32 v8, 16, v12
	global_load_dwordx4 v[138:141], v[138:139], off
	v_and_b32_e32 v9, 0xffff0000, v12
	v_pk_fma_f32 v[6:7], v[6:7], s[14:15], v[8:9] op_sel_hi:[1,0,1]
	s_waitcnt vmcnt(5)
	v_lshlrev_b32_e32 v59, 16, v19
	s_waitcnt vmcnt(4)
	v_lshlrev_b32_e32 v8, 16, v20
	v_and_b32_e32 v9, 0xffff0000, v20
	v_pk_add_f32 v[6:7], v[6:7], v[8:9]
	v_lshlrev_b32_e32 v8, 16, v122
	v_and_b32_e32 v9, 0xffff0000, v122
	v_pk_add_f32 v[6:7], v[6:7], v[8:9]
	v_lshlrev_b32_e32 v8, 16, v126
	v_and_b32_e32 v9, 0xffff0000, v126
	v_pk_add_f32 v[6:7], v[6:7], v[8:9]
	v_lshlrev_b32_e32 v8, 16, v13
	v_and_b32_e32 v9, 0xffff0000, v13
	v_pk_fma_f32 v[8:9], v[10:11], s[14:15], v[8:9] op_sel_hi:[1,0,1]
	v_lshlrev_b32_e32 v10, 16, v21
	v_and_b32_e32 v11, 0xffff0000, v21
	v_pk_add_f32 v[8:9], v[8:9], v[10:11]
	v_lshlrev_b32_e32 v10, 16, v123
	v_and_b32_e32 v11, 0xffff0000, v123
	v_pk_add_f32 v[8:9], v[8:9], v[10:11]
	v_lshlrev_b32_e32 v10, 16, v127
	v_and_b32_e32 v11, 0xffff0000, v127
	v_pk_add_f32 v[8:9], v[8:9], v[10:11]
	v_lshlrev_b32_e32 v10, 16, v14
	v_and_b32_e32 v11, 0xffff0000, v14
	v_pk_fma_f32 v[10:11], v[86:87], s[14:15], v[10:11] op_sel_hi:[1,0,1]
	v_lshlrev_b32_e32 v12, 16, v22
	v_and_b32_e32 v13, 0xffff0000, v22
	v_pk_add_f32 v[10:11], v[10:11], v[12:13]
	v_lshlrev_b32_e32 v12, 16, v124
	v_and_b32_e32 v13, 0xffff0000, v124
	v_pk_add_f32 v[10:11], v[10:11], v[12:13]
	v_lshlrev_b32_e32 v12, 16, v128
	v_and_b32_e32 v13, 0xffff0000, v128
	v_pk_add_f32 v[10:11], v[10:11], v[12:13]
	v_lshlrev_b32_e32 v12, 16, v15
	v_and_b32_e32 v13, 0xffff0000, v15
	v_pk_fma_f32 v[12:13], v[142:143], s[14:15], v[12:13] op_sel_hi:[1,0,1]
	v_lshlrev_b32_e32 v14, 16, v23
	v_and_b32_e32 v15, 0xffff0000, v23
	v_pk_add_f32 v[12:13], v[12:13], v[14:15]
	v_lshlrev_b32_e32 v14, 16, v125
	v_and_b32_e32 v15, 0xffff0000, v125
	v_pk_add_f32 v[12:13], v[12:13], v[14:15]
	v_lshlrev_b32_e32 v14, 16, v129
	v_and_b32_e32 v15, 0xffff0000, v129
	v_pk_add_f32 v[12:13], v[12:13], v[14:15]
	v_lshlrev_b32_e32 v20, 16, v16
	v_and_b32_e32 v16, 0xffff0000, v16
	v_lshlrev_b32_e32 v14, 16, v17
	v_and_b32_e32 v15, 0xffff0000, v17
	v_pk_add_f32 v[86:87], v[8:9], v[8:9] op_sel:[0,1] op_sel_hi:[1,0]
	v_sub_f32_e32 v15, v15, v82
	v_sub_f32_e32 v14, v14, v82
	v_sub_f32_e32 v17, v16, v82
	v_sub_f32_e32 v16, v20, v82
	v_pk_add_f32 v[22:23], v[6:7], v[6:7] op_sel:[0,1] op_sel_hi:[1,0]
	v_and_b32_e32 v87, 0xffff0000, v19
	v_pk_mul_f32 v[16:17], v[82:83], v[16:17] op_sel:[1,0]
	v_pk_mul_f32 v[14:15], v[82:83], v[14:15] op_sel:[1,0]
	v_lshlrev_b32_e32 v23, 16, v18
	v_and_b32_e32 v21, 0xffff0000, v18
	s_waitcnt vmcnt(4)
; DI void p7_ln2(const Ctx& c) {
;     ...
;             z[2 * i] = a0; z[2 * i + 1] = a1; s += ((a0[0] + a0[1]) + (a0[2] + a0[3])) + ((a1[0] + a1[1]) + (a1[2] + a1[3])); }
; #pragma unroll
;         for (int o = 32; o >= 1; o >>= 1) s += __shfl_xor(s, o);
;         const float mean = s * (1.0f / D); float qv = 0.f;
; #pragma unroll
;         for (int i = 0; i < 8; ++i) { const f32x4 dl = z[i] - mean; qv += (dl[0] * dl[0] + dl[1] * dl[1]) + (dl[2] * dl[2] + dl[3] * dl[3]); }
; #pragma unroll
;         for (int o = 32; o >= 1; o >>= 1) qv += __shfl_xor(qv, o);
	v_pk_fma_f32 v[18:19], v[174:175], v[14:15], v[182:183]
	v_pk_fma_f32 v[14:15], v[172:173], v[16:17], v[180:181]
	v_sub_f32_e32 v17, v87, v82
	v_sub_f32_e32 v16, v59, v82
	v_sub_f32_e32 v21, v21, v82
	v_sub_f32_e32 v20, v23, v82
	v_pk_mul_f32 v[16:17], v[82:83], v[16:17] op_sel:[1,0]
	v_pk_mul_f32 v[20:21], v[82:83], v[20:21] op_sel:[1,0]
	v_pk_fma_f32 v[82:83], v[170:171], v[16:17], v[178:179]
	s_waitcnt vmcnt(3)
	v_lshlrev_b32_e32 v16, 16, v118
	v_and_b32_e32 v17, 0xffff0000, v118
	v_pk_fma_f32 v[14:15], v[14:15], s[14:15], v[16:17] op_sel_hi:[1,0,1]
	s_waitcnt vmcnt(2)
	v_lshlrev_b32_e32 v16, 16, v130
	v_and_b32_e32 v17, 0xffff0000, v130
	v_pk_add_f32 v[14:15], v[14:15], v[16:17]
	s_waitcnt vmcnt(1)
	v_lshlrev_b32_e32 v16, 16, v134
	v_and_b32_e32 v17, 0xffff0000, v134
	v_pk_add_f32 v[14:15], v[14:15], v[16:17]
	s_waitcnt vmcnt(0)
	v_lshlrev_b32_e32 v16, 16, v138
	v_and_b32_e32 v17, 0xffff0000, v138
	v_pk_add_f32 v[14:15], v[14:15], v[16:17]
	v_lshlrev_b32_e32 v16, 16, v119
	v_and_b32_e32 v17, 0xffff0000, v119
	v_pk_fma_f32 v[16:17], v[18:19], s[14:15], v[16:17] op_sel_hi:[1,0,1]
	v_lshlrev_b32_e32 v18, 16, v131
	v_and_b32_e32 v19, 0xffff0000, v131
	v_pk_add_f32 v[16:17], v[16:17], v[18:19]
	v_lshlrev_b32_e32 v18, 16, v135
	v_and_b32_e32 v19, 0xffff0000, v135
	v_pk_add_f32 v[16:17], v[16:17], v[18:19]
	v_lshlrev_b32_e32 v18, 16, v139
	v_and_b32_e32 v19, 0xffff0000, v139
	v_pk_fma_f32 v[20:21], v[168:169], v[20:21], v[176:177]
	v_pk_add_f32 v[16:17], v[16:17], v[18:19]
	v_lshlrev_b32_e32 v18, 16, v120
	v_and_b32_e32 v19, 0xffff0000, v120
	v_pk_fma_f32 v[18:19], v[20:21], s[14:15], v[18:19] op_sel_hi:[1,0,1]
	v_lshlrev_b32_e32 v20, 16, v132
	v_and_b32_e32 v21, 0xffff0000, v132
	v_pk_add_f32 v[18:19], v[18:19], v[20:21]
	v_lshlrev_b32_e32 v20, 16, v136
	v_and_b32_e32 v21, 0xffff0000, v136
	v_pk_add_f32 v[18:19], v[18:19], v[20:21]
	v_lshlrev_b32_e32 v20, 16, v140
	v_and_b32_e32 v21, 0xffff0000, v140
	v_pk_add_f32 v[18:19], v[18:19], v[20:21]
	v_lshlrev_b32_e32 v20, 16, v121
	v_and_b32_e32 v21, 0xffff0000, v121
	v_pk_fma_f32 v[20:21], v[82:83], s[14:15], v[20:21] op_sel_hi:[1,0,1]
	v_lshlrev_b32_e32 v82, 16, v133
	v_and_b32_e32 v83, 0xffff0000, v133
	v_pk_add_f32 v[20:21], v[20:21], v[82:83]
	v_lshlrev_b32_e32 v82, 16, v137
	v_and_b32_e32 v83, 0xffff0000, v137
	v_pk_add_f32 v[122:123], v[10:11], v[10:11] op_sel:[0,1] op_sel_hi:[1,0]
	v_pk_add_f32 v[124:125], v[12:13], v[12:13] op_sel:[0,1] op_sel_hi:[1,0]
	v_pk_add_f32 v[20:21], v[20:21], v[82:83]
	v_lshlrev_b32_e32 v82, 16, v141
	v_and_b32_e32 v83, 0xffff0000, v141
	v_pk_add_f32 v[20:21], v[20:21], v[82:83]
	v_mov_b32_e32 v123, v14
	v_mov_b32_e32 v125, v15
	v_mov_b32_e32 v23, v16
	v_mov_b32_e32 v87, v17
	v_pk_add_f32 v[82:83], v[122:123], v[124:125]
	v_pk_add_f32 v[22:23], v[22:23], v[86:87]
	v_mov_b32_e32 v89, v18
	v_mov_b32_e32 v59, v19
	v_mov_b32_e32 v93, v20
	v_mov_b32_e32 v91, v21
	v_pk_add_f32 v[22:23], v[82:83], v[22:23]
	v_pk_add_f32 v[82:83], v[88:89], v[58:59]
	v_pk_add_f32 v[86:87], v[92:93], v[90:91]
	s_nop 0
	v_pk_add_f32 v[82:83], v[82:83], v[86:87]
	s_nop 0
	v_pk_add_f32 v[22:23], v[82:83], v[22:23]
	s_nop 0
	v_add_f32_e32 v22, v22, v23
	ds_bpermute_b32 v23, v94, v22
	s_waitcnt lgkmcnt(0)
	v_add_f32_e32 v22, v22, v23
	ds_bpermute_b32 v23, v95, v22
	s_waitcnt lgkmcnt(0)
	v_add_f32_e32 v22, v22, v23
	s_nop 1
	v_add_f32_dpp v22, v22, v22 row_ror:8 row_mask:0xf bank_mask:0xf
	s_nop 1
	v_add_f32_dpp v22, v22, v22 row_ror:4 row_mask:0xf bank_mask:0xf
	s_nop 1
	v_add_f32_dpp v22, v22, v22 quad_perm:[2,3,0,1] row_mask:0xf bank_mask:0xf
	s_nop 1
	v_add_f32_dpp v59, v22, v22 quad_perm:[1,0,3,2] row_mask:0xf bank_mask:0xf
	v_fmamk_f32 v75, v59, 0xba000000, v75
	v_fmamk_f32 v79, v59, 0xba000000, v79
	v_fmamk_f32 v77, v59, 0xba000000, v77
	v_fmac_f32_e32 v74, 0xba000000, v59
	v_fmamk_f32 v81, v59, 0xba000000, v81
	v_fmac_f32_e32 v78, 0xba000000, v59
	v_mov_b32_e32 v82, v75
	v_mov_b32_e32 v83, v79
	v_fmac_f32_e32 v76, 0xba000000, v59
	v_fmac_f32_e32 v80, 0xba000000, v59
	v_mov_b32_e32 v22, v74
	v_mov_b32_e32 v23, v78
	v_pk_mul_f32 v[82:83], v[82:83], v[82:83]
	v_mov_b32_e32 v86, v77
	v_mov_b32_e32 v87, v81
	v_pk_fma_f32 v[22:23], v[22:23], v[22:23], v[82:83]
	v_mov_b32_e32 v82, v76
	v_mov_b32_e32 v83, v80
	v_pk_mul_f32 v[86:87], v[86:87], v[86:87]
	v_fmamk_f32 v85, v59, 0xba000000, v85
	v_pk_fma_f32 v[82:83], v[82:83], v[82:83], v[86:87]
	v_fmac_f32_e32 v84, 0xba000000, v59
	v_pk_add_f32 v[22:23], v[22:23], v[82:83]
	v_fmamk_f32 v1, v59, 0xba000000, v1
	v_fmac_f32_e32 v0, 0xba000000, v59
	v_pk_add_f32 v[22:23], v[22:23], v[22:23] op_sel_hi:[0,1]
	v_pk_mul_f32 v[82:83], v[0:1], v[0:1]
	v_pk_mul_f32 v[86:87], v[84:85], v[84:85]
	v_fmac_f32_e32 v4, 0xba000000, v59
	v_pk_mov_b32 v[88:89], v[86:87], v[82:83] op_sel:[1,0]
	v_mov_b32_e32 v87, v83
	v_fmamk_f32 v5, v59, 0xba000000, v5
	v_fmac_f32_e32 v2, 0xba000000, v59
	v_mul_f32_e32 v22, v4, v4
	v_pk_add_f32 v[82:83], v[88:89], v[86:87]
	v_fmamk_f32 v3, v59, 0xba000000, v3
	v_pk_fma_f32 v[86:87], v[4:5], v[4:5], v[22:23] op_sel_hi:[1,1,0]
	v_mul_f32_e32 v22, v2, v2
	v_pk_add_f32 v[82:83], v[82:83], v[82:83] op_sel_hi:[0,1]
	v_pk_fma_f32 v[88:89], v[2:3], v[2:3], v[22:23] op_sel_hi:[1,1,0]
	v_fmamk_f32 v9, v59, 0xba000000, v9
	v_fmac_f32_e32 v8, 0xba000000, v59
	v_fmamk_f32 v7, v59, 0xba000000, v7
	v_fmac_f32_e32 v6, 0xba000000, v59
	v_mul_f32_e32 v86, v6, v6
	v_mul_f32_e32 v88, v7, v7
	v_mul_f32_e32 v82, v8, v8
	v_mul_f32_e32 v22, v9, v9
	v_pk_add_f32 v[86:87], v[86:87], v[88:89]
	v_pk_add_f32 v[22:23], v[82:83], v[22:23]
	v_fmamk_f32 v11, v59, 0xba000000, v11
	v_pk_add_f32 v[22:23], v[86:87], v[22:23]
	v_fmac_f32_e32 v10, 0xba000000, v59
	v_fmamk_f32 v13, v59, 0xba000000, v13
	v_fmac_f32_e32 v12, 0xba000000, v59
	v_pk_add_f32 v[22:23], v[22:23], v[22:23] op_sel_hi:[0,1]
	v_pk_mul_f32 v[82:83], v[12:13], v[12:13]
	v_pk_mul_f32 v[110:111], v[10:11], v[10:11]
	v_fmac_f32_e32 v14, 0xba000000, v59
	v_pk_mov_b32 v[112:113], v[110:111], v[82:83] op_sel:[1,0]
	v_mov_b32_e32 v111, v83
	v_fmamk_f32 v15, v59, 0xba000000, v15
	v_fmac_f32_e32 v16, 0xba000000, v59
	v_mul_f32_e32 v22, v14, v14
	v_pk_add_f32 v[82:83], v[112:113], v[110:111]
	v_fmamk_f32 v17, v59, 0xba000000, v17
	v_pk_fma_f32 v[110:111], v[14:15], v[14:15], v[22:23] op_sel_hi:[1,1,0]
	v_mul_f32_e32 v22, v16, v16
	v_pk_add_f32 v[82:83], v[82:83], v[82:83] op_sel_hi:[0,1]
	v_pk_fma_f32 v[112:113], v[16:17], v[16:17], v[22:23] op_sel_hi:[1,1,0]
	v_fmamk_f32 v21, v59, 0xba000000, v21
	v_fmac_f32_e32 v20, 0xba000000, v59
	v_fmamk_f32 v19, v59, 0xba000000, v19
	v_fmac_f32_e32 v18, 0xba000000, v59
	v_mul_f32_e32 v110, v18, v18
	v_mul_f32_e32 v112, v19, v19
	v_mul_f32_e32 v82, v20, v20
	v_mul_f32_e32 v22, v21, v21
	v_pk_add_f32 v[110:111], v[110:111], v[112:113]
	v_pk_add_f32 v[22:23], v[82:83], v[22:23]
	s_nop 0
	v_pk_add_f32 v[22:23], v[110:111], v[22:23]
	s_nop 0
	v_add_f32_e32 v22, v22, v23
	ds_bpermute_b32 v23, v94, v22
	s_waitcnt lgkmcnt(0)
; DI u32x2 pack4(f32x4 v) { bf16x4_t r = __builtin_convertvector(v, bf16x4_t); return __builtin_bit_cast(u32x2, r); }
; DI void p7_ln2(const Ctx& c) {
;     ...
;         const float rstd = rsqrtf(qv * (1.0f / D) + LN_EPS);
; #pragma unroll
;         for (int i = 0; i < 4; ++i) { const int d = (i * 64 + lane) * 8;
;             const f32x4 g0 = *(const f32x4*)(l2w + d), g1 = *(const f32x4*)(l2w + d + 4), b0 = *(const f32x4*)(l2b + d), b1 = *(const f32x4*)(l2b + d + 4);
;             const u32x2 lo = pack4((z[2 * i] - mean) * rstd * g0 + b0), hi = pack4((z[2 * i + 1] - mean) * rstd * g1 + b1);
;             *(u32x4*)(x2b + (size_t)tok * D + d) = (u32x4){lo.x, lo.y, hi.x, hi.y}; }
;         float q2 = (lane < 32) ? ssq[(size_t)tok * 32 + lane] : 0.f;
; #pragma unroll
;         for (int o = 32; o >= 1; o >>= 1) q2 += __shfl_xor(q2, o);
;         if (lane == 0) rse[tok] = rsqrtf(q2 * (1.0f / D) + LN_EPS); }
	v_add_f32_e32 v22, v22, v23
	ds_bpermute_b32 v23, v95, v22
	s_waitcnt lgkmcnt(0)
	v_add_f32_e32 v22, v22, v23
	s_nop 1
	v_add_f32_dpp v22, v22, v22 row_ror:8 row_mask:0xf bank_mask:0xf
	s_nop 1
	v_add_f32_dpp v22, v22, v22 row_ror:4 row_mask:0xf bank_mask:0xf
	s_nop 1
	v_add_f32_dpp v22, v22, v22 quad_perm:[2,3,0,1] row_mask:0xf bank_mask:0xf
	s_nop 1
	v_add_f32_dpp v22, v22, v22 quad_perm:[1,0,3,2] row_mask:0xf bank_mask:0xf
	v_fmamk_f32 v22, v22, 0x3a000000, v100
	v_mul_f32_e32 v23, 0x4b800000, v22
	v_cmp_gt_f32_e64 s[10:11], s27, v22
	s_nop 1
	v_cndmask_b32_e64 v22, v22, v23, s[10:11]
	v_rsq_f32_e32 v22, v22
	s_nop 0
	v_mul_f32_e32 v23, 0x45800000, v22
	v_cndmask_b32_e64 v22, v22, v23, s[10:11]
	v_pk_mul_f32 v[76:77], v[76:77], v[22:23] op_sel_hi:[1,0]
	v_pk_mul_f32 v[74:75], v[74:75], v[22:23] op_sel_hi:[1,0]
	v_pk_mul_f32 v[78:79], v[78:79], v[22:23] op_sel_hi:[1,0]
	s_waitcnt vmcnt(0)
	v_pk_fma_f32 v[82:83], v[188:189], v[74:75], v[196:197]
	v_pk_fma_f32 v[74:75], v[190:191], v[76:77], v[198:199]
	v_pk_mul_f32 v[76:77], v[80:81], v[22:23] op_sel_hi:[1,0]
	v_pk_fma_f32 v[78:79], v[184:185], v[78:79], v[192:193]
	v_pk_fma_f32 v[76:77], v[186:187], v[76:77], v[194:195]
	v_add_co_u32_e64 v90, s[10:11], s28, v72
	v_cvt_pk_bf16_f32 v75, v74, v75
	v_cvt_pk_bf16_f32 v74, v82, v83
	v_cvt_pk_bf16_f32 v77, v76, v77
	v_cvt_pk_bf16_f32 v76, v78, v79
	v_addc_co_u32_e64 v91, s[10:11], 0, v73, s[10:11]
	global_store_dwordx4 v[90:91], v[74:77], off
	s_nop 0
	v_pk_mul_f32 v[84:85], v[84:85], v[22:23] op_sel_hi:[1,0]
	v_pk_mul_f32 v[0:1], v[0:1], v[22:23] op_sel_hi:[1,0]
	v_pk_mul_f32 v[4:5], v[4:5], v[22:23] op_sel_hi:[1,0]
	v_pk_mul_f32 v[2:3], v[2:3], v[22:23] op_sel_hi:[1,0]
	s_waitcnt vmcnt(1)
	v_pk_fma_f32 v[74:75], v[206:207], v[0:1], v[202:203]
	v_pk_fma_f32 v[0:1], v[204:205], v[84:85], v[200:201]
	s_waitcnt vmcnt(1)
	v_pk_fma_f32 v[72:73], v[210:211], v[2:3], v[218:219]
	v_pk_fma_f32 v[2:3], v[208:209], v[4:5], v[216:217]
	v_cvt_pk_bf16_f32 v0, v0, v1
	v_cvt_pk_bf16_f32 v1, v74, v75
	v_cvt_pk_bf16_f32 v2, v2, v3
	v_cvt_pk_bf16_f32 v3, v72, v73
	global_store_dwordx4 v[90:91], v[0:3], off offset:1024
	s_nop 0
	v_pk_mul_f32 v[4:5], v[6:7], v[22:23] op_sel_hi:[1,0]
	v_pk_mul_f32 v[6:7], v[8:9], v[22:23] op_sel_hi:[1,0]
	s_waitcnt vmcnt(2)
	v_pk_fma_f32 v[0:1], v[224:225], v[4:5], v[220:221]
	v_pk_fma_f32 v[2:3], v[226:227], v[6:7], v[222:223]
	v_cvt_pk_bf16_f32 v0, v0, v1
	v_cvt_pk_bf16_f32 v1, v2, v3
	v_pk_mul_f32 v[2:3], v[10:11], v[22:23] op_sel_hi:[1,0]
	v_pk_mul_f32 v[4:5], v[12:13], v[22:23] op_sel_hi:[1,0]
	s_waitcnt vmcnt(2)
	v_pk_fma_f32 v[2:3], v[230:231], v[2:3], v[234:235]
	v_pk_fma_f32 v[4:5], v[232:233], v[4:5], v[236:237]
	v_cvt_pk_bf16_f32 v2, v2, v3
	v_cvt_pk_bf16_f32 v3, v4, v5
	global_store_dwordx4 v[90:91], v[0:3], off offset:2048
	s_nop 0
	v_pk_mul_f32 v[12:13], v[14:15], v[22:23] op_sel_hi:[1,0]
	v_pk_mul_f32 v[14:15], v[16:17], v[22:23] op_sel_hi:[1,0]
	s_waitcnt vmcnt(3)
	v_pk_fma_f32 v[0:1], v[244:245], v[12:13], v[238:239]
	v_pk_fma_f32 v[2:3], v[246:247], v[14:15], v[240:241]
	v_cvt_pk_bf16_f32 v0, v0, v1
	v_cvt_pk_bf16_f32 v1, v2, v3
	v_pk_mul_f32 v[2:3], v[18:19], v[22:23] op_sel_hi:[1,0]
	v_pk_mul_f32 v[4:5], v[20:21], v[22:23] op_sel_hi:[1,0]
	s_waitcnt vmcnt(3)
	v_pk_fma_f32 v[2:3], v[248:249], v[2:3], v[252:253]
	v_pk_fma_f32 v[4:5], v[250:251], v[4:5], v[254:255]
	v_cvt_pk_bf16_f32 v2, v2, v3
	v_cvt_pk_bf16_f32 v3, v4, v5
	global_store_dwordx4 v[90:91], v[0:3], off offset:3072
	s_nop 1
	v_mov_b32_e32 v0, 0
	s_and_saveexec_b64 s[10:11], vcc
	s_cbranch_execz .LBB0_979
	v_lshl_add_u64 v[0:1], s[34:35], 0, v[60:61]
	global_load_dword v0, v[0:1], off
.LBB0_979:
	s_or_b64 exec, exec, s[10:11]
	s_waitcnt vmcnt(0)
	ds_bpermute_b32 v1, v94, v0
	s_waitcnt lgkmcnt(0)
	v_add_f32_e32 v0, v0, v1
	ds_bpermute_b32 v1, v95, v0
	s_waitcnt lgkmcnt(0)
	v_add_f32_e32 v0, v0, v1
	s_nop 1
	v_add_f32_dpp v0, v0, v0 row_ror:8 row_mask:0xf bank_mask:0xf
	s_nop 1
	v_add_f32_dpp v0, v0, v0 row_ror:4 row_mask:0xf bank_mask:0xf
	s_nop 1
	v_add_f32_dpp v0, v0, v0 quad_perm:[2,3,0,1] row_mask:0xf bank_mask:0xf
	ds_bpermute_b32 v1, v99, v0
	s_and_saveexec_b64 s[22:23], s[6:7]
	s_cbranch_execz .LBB0_976
	s_waitcnt lgkmcnt(0)
	v_add_f32_e32 v0, v0, v1
	v_fmamk_f32 v0, v0, 0x3a000000, v100
	v_mul_f32_e32 v1, 0x4b800000, v0
	v_cmp_gt_f32_e64 s[10:11], s27, v0
	s_add_u32 s36, s34, s30
	s_addc_u32 s37, s35, s31
	v_cndmask_b32_e64 v0, v0, v1, s[10:11]
	v_rsq_f32_e32 v0, v0
	s_nop 0
	v_mul_f32_e32 v1, 0x45800000, v0
	v_cndmask_b32_e64 v0, v0, v1, s[10:11]
	global_store_dword v58, v0, s[36:37]
	s_branch .LBB0_976
